# v31 + down-GEMM epilogue: 32 redundant zero-init v_mov before cvt_pk_fp8 lo/hi pairs removed (both fp8 epilogues are VALU-throughput-bound)
# baseline (speedup 1.0000x reference)
.LBB0_52:
	s_nop 15
	s_nop 15
	v_lshl_add_u32 v22, s62, 8, v186
	v_ashrrev_i32_e32 v23, 31, v22
	s_ashr_i32 s27, s26, 31
	s_andn2_b64 vcc, exec, s[54:55]
	s_waitcnt vmcnt(0)
	v_pk_fma_f32 v[28:29], v[154:155], s[24:25], v[10:11] op_sel_hi:[1,0,1]
	v_pk_fma_f32 v[24:25], v[158:159], s[24:25], v[14:15] op_sel_hi:[1,0,1]
	v_cvt_pk_fp8_f32 v19, v28, v29
	v_cvt_pk_fp8_f32 v18, v24, v25
	v_pk_fma_f32 v[20:21], v[160:161], s[24:25], v[16:17] op_sel_hi:[1,0,1]
	v_pk_fma_f32 v[26:27], v[156:157], s[24:25], v[12:13] op_sel_hi:[1,0,1]
	v_pk_fma_f32 v[30:31], v[146:147], s[24:25], v[10:11] op_sel_hi:[1,0,1]
	v_cvt_pk_fp8_f32 v18, v20, v21 op_sel:[0,0,1]
	v_cvt_pk_fp8_f32 v19, v26, v27 op_sel:[0,0,1]
	v_pk_fma_f32 v[26:27], v[150:151], s[24:25], v[14:15] op_sel_hi:[1,0,1]
	v_cvt_pk_fp8_f32 v20, v26, v27
	v_cvt_pk_fp8_f32 v21, v30, v31
	v_pk_fma_f32 v[24:25], v[152:153], s[24:25], v[16:17] op_sel_hi:[1,0,1]
	v_pk_fma_f32 v[28:29], v[148:149], s[24:25], v[12:13] op_sel_hi:[1,0,1]
	v_cvt_pk_fp8_f32 v20, v24, v25 op_sel:[0,0,1]
	v_cvt_pk_fp8_f32 v21, v28, v29 op_sel:[0,0,1]
	v_lshlrev_b64 v[24:25], 10, v[22:23]
	v_lshl_add_u64 v[24:25], s[40:41], 0, v[24:25]
	v_lshl_add_u64 v[24:25], v[24:25], 0, s[26:27]
	v_lshl_add_u64 v[24:25], v[24:25], 0, s[94:95]
	v_permlane16_swap_b32_e32 v18, v20
	v_permlane16_swap_b32_e32 v19, v21
	v_lshl_add_u64 v[24:25], v[24:25], 0, v[168:169]
	global_store_dwordx4 v[24:25], v[18:21], off
	v_pk_fma_f32 v[26:27], v[142:143], s[24:25], v[6:7] op_sel_hi:[1,0,1]
	v_pk_fma_f32 v[30:31], v[138:139], s[24:25], v[2:3] op_sel_hi:[1,0,1]
	v_cvt_pk_fp8_f32 v18, v26, v27
	v_cvt_pk_fp8_f32 v19, v30, v31
	v_pk_fma_f32 v[20:21], v[144:145], s[24:25], v[8:9] op_sel_hi:[1,0,1]
	v_pk_fma_f32 v[28:29], v[140:141], s[24:25], v[4:5] op_sel_hi:[1,0,1]
	v_cvt_pk_fp8_f32 v18, v20, v21 op_sel:[0,0,1]
	v_cvt_pk_fp8_f32 v19, v28, v29 op_sel:[0,0,1]
	v_pk_fma_f32 v[28:29], v[134:135], s[24:25], v[6:7] op_sel_hi:[1,0,1]
	v_pk_fma_f32 v[32:33], v[130:131], s[24:25], v[2:3] op_sel_hi:[1,0,1]
	v_cvt_pk_fp8_f32 v20, v28, v29
	v_cvt_pk_fp8_f32 v21, v32, v33
	v_pk_fma_f32 v[26:27], v[136:137], s[24:25], v[8:9] op_sel_hi:[1,0,1]
	v_pk_fma_f32 v[30:31], v[132:133], s[24:25], v[4:5] op_sel_hi:[1,0,1]
	v_cvt_pk_fp8_f32 v20, v26, v27 op_sel:[0,0,1]
	v_cvt_pk_fp8_f32 v21, v30, v31 op_sel:[0,0,1]
	v_pk_fma_f32 v[26:27], v[126:127], s[24:25], v[14:15] op_sel_hi:[1,0,1]
	v_pk_fma_f32 v[30:31], v[122:123], s[24:25], v[10:11] op_sel_hi:[1,0,1]
	v_permlane16_swap_b32_e32 v18, v20
	v_permlane16_swap_b32_e32 v19, v21
	global_store_dwordx4 v[24:25], v[18:21], off offset:128
	v_pk_fma_f32 v[32:33], v[114:115], s[24:25], v[10:11] op_sel_hi:[1,0,1]
	v_or_b32_e32 v24, 32, v22
	v_cvt_pk_fp8_f32 v18, v26, v27
	v_pk_fma_f32 v[20:21], v[128:129], s[24:25], v[16:17] op_sel_hi:[1,0,1]
	v_cvt_pk_fp8_f32 v19, v30, v31
	v_cvt_pk_fp8_f32 v18, v20, v21 op_sel:[0,0,1]
	v_pk_fma_f32 v[30:31], v[118:119], s[24:25], v[14:15] op_sel_hi:[1,0,1]
	v_cvt_pk_fp8_f32 v20, v30, v31
	v_cvt_pk_fp8_f32 v21, v32, v33
	v_pk_fma_f32 v[28:29], v[124:125], s[24:25], v[12:13] op_sel_hi:[1,0,1]
	v_ashrrev_i32_e32 v25, 31, v24
	v_cvt_pk_fp8_f32 v19, v28, v29 op_sel:[0,0,1]
	v_pk_fma_f32 v[28:29], v[120:121], s[24:25], v[16:17] op_sel_hi:[1,0,1]
	v_pk_fma_f32 v[26:27], v[116:117], s[24:25], v[12:13] op_sel_hi:[1,0,1]
	v_cvt_pk_fp8_f32 v20, v28, v29 op_sel:[0,0,1]
	v_cvt_pk_fp8_f32 v21, v26, v27 op_sel:[0,0,1]
	v_lshlrev_b64 v[24:25], 10, v[24:25]
	v_lshl_add_u64 v[24:25], s[40:41], 0, v[24:25]
	v_lshl_add_u64 v[24:25], v[24:25], 0, s[26:27]
	v_lshl_add_u64 v[24:25], v[24:25], 0, s[94:95]
	v_permlane16_swap_b32_e32 v18, v20
	v_permlane16_swap_b32_e32 v19, v21
	v_lshl_add_u64 v[24:25], v[24:25], 0, v[168:169]
	global_store_dwordx4 v[24:25], v[18:21], off
	v_pk_fma_f32 v[26:27], v[110:111], s[24:25], v[6:7] op_sel_hi:[1,0,1]
	v_pk_fma_f32 v[30:31], v[106:107], s[24:25], v[2:3] op_sel_hi:[1,0,1]
	v_cvt_pk_fp8_f32 v18, v26, v27
	v_cvt_pk_fp8_f32 v19, v30, v31
	v_pk_fma_f32 v[20:21], v[112:113], s[24:25], v[8:9] op_sel_hi:[1,0,1]
	v_pk_fma_f32 v[28:29], v[108:109], s[24:25], v[4:5] op_sel_hi:[1,0,1]
	v_cvt_pk_fp8_f32 v18, v20, v21 op_sel:[0,0,1]
	v_cvt_pk_fp8_f32 v19, v28, v29 op_sel:[0,0,1]
	v_pk_fma_f32 v[28:29], v[102:103], s[24:25], v[6:7] op_sel_hi:[1,0,1]
	v_pk_fma_f32 v[32:33], v[98:99], s[24:25], v[2:3] op_sel_hi:[1,0,1]
	v_cvt_pk_fp8_f32 v20, v28, v29
	v_cvt_pk_fp8_f32 v21, v32, v33
	v_pk_fma_f32 v[26:27], v[104:105], s[24:25], v[8:9] op_sel_hi:[1,0,1]
	v_pk_fma_f32 v[30:31], v[100:101], s[24:25], v[4:5] op_sel_hi:[1,0,1]
	v_cvt_pk_fp8_f32 v20, v26, v27 op_sel:[0,0,1]
	v_cvt_pk_fp8_f32 v21, v30, v31 op_sel:[0,0,1]
	v_pk_fma_f32 v[26:27], v[94:95], s[24:25], v[14:15] op_sel_hi:[1,0,1]
	v_pk_fma_f32 v[30:31], v[90:91], s[24:25], v[10:11] op_sel_hi:[1,0,1]
	v_permlane16_swap_b32_e32 v18, v20
	v_permlane16_swap_b32_e32 v19, v21
	global_store_dwordx4 v[24:25], v[18:21], off offset:128
	v_pk_fma_f32 v[28:29], v[92:93], s[24:25], v[12:13] op_sel_hi:[1,0,1]
	v_pk_fma_f32 v[32:33], v[82:83], s[24:25], v[10:11] op_sel_hi:[1,0,1]
	v_cvt_pk_fp8_f32 v18, v26, v27
	v_cvt_pk_fp8_f32 v19, v30, v31
	v_pk_fma_f32 v[20:21], v[96:97], s[24:25], v[16:17] op_sel_hi:[1,0,1]
	v_add_u32_e32 v24, 0x80, v22
	v_cvt_pk_fp8_f32 v18, v20, v21 op_sel:[0,0,1]
	v_cvt_pk_fp8_f32 v19, v28, v29 op_sel:[0,0,1]
	v_pk_fma_f32 v[28:29], v[86:87], s[24:25], v[14:15] op_sel_hi:[1,0,1]
	v_cvt_pk_fp8_f32 v20, v28, v29
	v_cvt_pk_fp8_f32 v21, v32, v33
	v_ashrrev_i32_e32 v25, 31, v24
	v_pk_fma_f32 v[26:27], v[88:89], s[24:25], v[16:17] op_sel_hi:[1,0,1]
	v_pk_fma_f32 v[30:31], v[84:85], s[24:25], v[12:13] op_sel_hi:[1,0,1]
	v_cvt_pk_fp8_f32 v20, v26, v27 op_sel:[0,0,1]
	v_cvt_pk_fp8_f32 v21, v30, v31 op_sel:[0,0,1]
	v_lshlrev_b64 v[24:25], 10, v[24:25]
	v_lshl_add_u64 v[24:25], s[40:41], 0, v[24:25]
	v_lshl_add_u64 v[24:25], v[24:25], 0, s[26:27]
	v_lshl_add_u64 v[24:25], v[24:25], 0, s[94:95]
	v_permlane16_swap_b32_e32 v18, v20
	v_permlane16_swap_b32_e32 v19, v21
	v_lshl_add_u64 v[24:25], v[24:25], 0, v[168:169]
	global_store_dwordx4 v[24:25], v[18:21], off
	v_pk_fma_f32 v[26:27], v[78:79], s[24:25], v[6:7] op_sel_hi:[1,0,1]
	v_pk_fma_f32 v[30:31], v[74:75], s[24:25], v[2:3] op_sel_hi:[1,0,1]
	v_cvt_pk_fp8_f32 v18, v26, v27
	v_cvt_pk_fp8_f32 v19, v30, v31
	v_pk_fma_f32 v[20:21], v[80:81], s[24:25], v[8:9] op_sel_hi:[1,0,1]
	v_pk_fma_f32 v[28:29], v[76:77], s[24:25], v[4:5] op_sel_hi:[1,0,1]
	v_cvt_pk_fp8_f32 v18, v20, v21 op_sel:[0,0,1]
	v_cvt_pk_fp8_f32 v19, v28, v29 op_sel:[0,0,1]
	v_pk_fma_f32 v[28:29], v[70:71], s[24:25], v[6:7] op_sel_hi:[1,0,1]
	v_pk_fma_f32 v[32:33], v[66:67], s[24:25], v[2:3] op_sel_hi:[1,0,1]
	v_cvt_pk_fp8_f32 v20, v28, v29
	v_cvt_pk_fp8_f32 v21, v32, v33
	v_pk_fma_f32 v[26:27], v[72:73], s[24:25], v[8:9] op_sel_hi:[1,0,1]
	v_pk_fma_f32 v[30:31], v[68:69], s[24:25], v[4:5] op_sel_hi:[1,0,1]
	v_cvt_pk_fp8_f32 v20, v26, v27 op_sel:[0,0,1]
	v_cvt_pk_fp8_f32 v21, v30, v31 op_sel:[0,0,1]
	v_add_u32_e32 v22, 0xa0, v22
	v_ashrrev_i32_e32 v23, 31, v22
	v_permlane16_swap_b32_e32 v18, v20
	v_permlane16_swap_b32_e32 v19, v21
	global_store_dwordx4 v[24:25], v[18:21], off offset:128
	v_pk_fma_f32 v[24:25], v[62:63], s[24:25], v[14:15] op_sel_hi:[1,0,1]
	v_pk_fma_f32 v[28:29], v[58:59], s[24:25], v[10:11] op_sel_hi:[1,0,1]
	v_cvt_pk_fp8_f32 v18, v24, v25
	v_pk_fma_f32 v[20:21], v[64:65], s[24:25], v[16:17] op_sel_hi:[1,0,1]
	v_pk_fma_f32 v[14:15], v[54:55], s[24:25], v[14:15] op_sel_hi:[1,0,1]
	v_cvt_pk_fp8_f32 v18, v20, v21 op_sel:[0,0,1]
	v_pk_fma_f32 v[10:11], v[50:51], s[24:25], v[10:11] op_sel_hi:[1,0,1]
	v_cvt_pk_fp8_f32 v19, v28, v29
	v_cvt_pk_fp8_f32 v20, v14, v15
	v_cvt_pk_fp8_f32 v21, v10, v11
	v_lshlrev_b64 v[10:11], 10, v[22:23]
	v_lshl_add_u64 v[10:11], s[40:41], 0, v[10:11]
	v_lshl_add_u64 v[10:11], v[10:11], 0, s[26:27]
	v_pk_fma_f32 v[26:27], v[60:61], s[24:25], v[12:13] op_sel_hi:[1,0,1]
	v_pk_fma_f32 v[16:17], v[56:57], s[24:25], v[16:17] op_sel_hi:[1,0,1]
	v_pk_fma_f32 v[12:13], v[52:53], s[24:25], v[12:13] op_sel_hi:[1,0,1]
	v_lshl_add_u64 v[10:11], v[10:11], 0, s[94:95]
	v_cvt_pk_fp8_f32 v19, v26, v27 op_sel:[0,0,1]
	v_cvt_pk_fp8_f32 v20, v16, v17 op_sel:[0,0,1]
	v_cvt_pk_fp8_f32 v21, v12, v13 op_sel:[0,0,1]
	v_lshl_add_u64 v[14:15], v[10:11], 0, v[168:169]
	v_pk_fma_f32 v[16:17], v[46:47], s[24:25], v[6:7] op_sel_hi:[1,0,1]
	v_cvt_pk_fp8_f32 v10, v16, v17
	v_permlane16_swap_b32_e32 v18, v20
	v_permlane16_swap_b32_e32 v19, v21
	v_pk_fma_f32 v[12:13], v[48:49], s[24:25], v[8:9] op_sel_hi:[1,0,1]
	global_store_dwordx4 v[14:15], v[18:21], off
	v_cvt_pk_fp8_f32 v10, v12, v13 op_sel:[0,0,1]
	v_pk_fma_f32 v[20:21], v[42:43], s[24:25], v[2:3] op_sel_hi:[1,0,1]
	v_pk_fma_f32 v[6:7], v[38:39], s[24:25], v[6:7] op_sel_hi:[1,0,1]
	v_pk_fma_f32 v[2:3], v[34:35], s[24:25], v[2:3] op_sel_hi:[1,0,1]
	v_cvt_pk_fp8_f32 v11, v20, v21
	v_cvt_pk_fp8_f32 v12, v6, v7
	v_cvt_pk_fp8_f32 v13, v2, v3
	v_pk_fma_f32 v[18:19], v[44:45], s[24:25], v[4:5] op_sel_hi:[1,0,1]
	v_pk_fma_f32 v[8:9], v[40:41], s[24:25], v[8:9] op_sel_hi:[1,0,1]
	v_pk_fma_f32 v[4:5], v[36:37], s[24:25], v[4:5] op_sel_hi:[1,0,1]
	v_cvt_pk_fp8_f32 v11, v18, v19 op_sel:[0,0,1]
	v_cvt_pk_fp8_f32 v12, v8, v9 op_sel:[0,0,1]
	v_cvt_pk_fp8_f32 v13, v4, v5 op_sel:[0,0,1]
	s_mov_b64 s[26:27], -1
	v_permlane16_swap_b32_e32 v10, v12
	v_permlane16_swap_b32_e32 v11, v13
	global_store_dwordx4 v[14:15], v[10:13], off offset:128
	s_cbranch_vccnz .LBB0_39
	s_andn2_b64 vcc, exec, s[38:39]
	s_cbranch_vccnz .LBB0_38
	s_barrier
	s_branch .LBB0_38
